# v11 with the PROJ start stagger over 8 groups (bid>>3)&7 in 2.7 us steps instead of 4 groups in 6.5 us steps
# speedup vs baseline: 1.0084x; 1.0008x over previous
.Lstg_loop_proj:
	s_sleep 90
	s_sub_u32 s2, s2, 1
	s_cmp_lg_u32 s2, 0
	s_cbranch_scc1 .Lstg_loop_proj
